# speedup vs baseline: 1.0034x; 1.0034x over previous
_Z8dog_mainPKfS0_S0_S0_S0_S0_S0_Pf:
	s_load_dwordx8 s[12:19], s[0:1], 0x0
	s_load_dwordx8 s[20:27], s[0:1], 0x20
	s_and_b32 s3, s2, 7
	s_lshl_b32 s3, s3, 5
	s_lshr_b32 s4, s2, 3
	s_add_i32 s4, s3, s4
	s_and_b32 s6, s4, 3
	s_lshr_b32 s7, s4, 2
	s_mov_b32 s5, 0
	s_lshl_b64 s[8:9], s[4:5], 18
	v_and_b32_e32 v1, 63, v0
	v_lshrrev_b32_e32 v2, 6, v0
	v_and_b32_e32 v3, 15, v0
	v_and_b32_e32 v7, 31, v0
	v_lshl_or_b32 v5, v2, 5, v7
	v_lshlrev_b32_e32 v5, 2, v5
	v_mov_b32_e32 v4, v5
	v_lshlrev_b32_e32 v6, 4, v1
	v_lshl_or_b32 v6, v2, 12, v6
	v_bfe_u32 v7, v0, 4, 2
	s_waitcnt lgkmcnt(0)
	global_load_dword v32, v4, s[18:19]
	global_load_dword v33, v4, s[20:21]
	global_load_dword v34, v4, s[22:23]
	global_load_dword v35, v4, s[24:25]
	global_load_dword v36, v4, s[14:15]
	global_load_dword v37, v4, s[16:17]
	s_add_u32 s12, s12, s8
	s_addc_u32 s13, s13, s9
	global_load_dwordx4 v[128:131], v6, s[12:13] offset:0 nt
	global_load_dwordx4 v[132:135], v6, s[12:13] offset:1024 nt
	global_load_dwordx4 v[136:139], v6, s[12:13] offset:2048 nt
	global_load_dwordx4 v[140:143], v6, s[12:13] offset:3072 nt
	v_add_u32_e32 v6, 0x8000, v6
	global_load_dwordx4 v[144:147], v6, s[12:13] offset:0 nt
	global_load_dwordx4 v[148:151], v6, s[12:13] offset:1024 nt
	global_load_dwordx4 v[152:155], v6, s[12:13] offset:2048 nt
	global_load_dwordx4 v[156:159], v6, s[12:13] offset:3072 nt
	v_add_u32_e32 v6, 0x8000, v6
	global_load_dwordx4 v[160:163], v6, s[12:13] offset:0 nt
	global_load_dwordx4 v[164:167], v6, s[12:13] offset:1024 nt
	global_load_dwordx4 v[168:171], v6, s[12:13] offset:2048 nt
	global_load_dwordx4 v[172:175], v6, s[12:13] offset:3072 nt
	v_and_b32_e32 v16, 1, v0
	v_cmp_eq_u32_e64 s[30:31], 0, v16
	v_and_b32_e32 v17, 2, v0
	v_cmp_eq_u32_e64 s[32:33], 0, v17
	v_and_b32_e32 v16, 3, v0
	v_lshrrev_b32_e32 v17, 2, v1
	v_lshlrev_b32_e32 v16, 5, v16
	v_lshl_add_u32 v16, v17, 1, v16
	v_lshrrev_b32_e32 v17, 1, v2
	s_movk_i32 s10, 0x110
	v_mad_u32_u24 v16, v17, s10, v16
	v_and_b32_e32 v17, 1, v2
	v_lshl_add_u32 v14, v17, 7, v16
	v_lshlrev_b32_e32 v17, 4, v7
	v_mad_u32_u24 v15, v3, s10, v17
	s_lshl_b32 s11, s6, 5
	v_lshl_add_u32 v18, v7, 2, s11
	v_cvt_f32_u32_e32 v18, v18
	v_lshlrev_b32_e32 v19, 3, v7
	v_cvt_f32_u32_e32 v19, v19
	s_waitcnt vmcnt(12)
	v_lshlrev_b32_e32 v16, 2, v3
	v_add_u32_e32 v17, 64, v16
	ds_bpermute_b32 v40, v16, v32
	ds_bpermute_b32 v46, v17, v32
	ds_bpermute_b32 v41, v16, v33
	ds_bpermute_b32 v47, v17, v33
	ds_bpermute_b32 v42, v16, v34
	ds_bpermute_b32 v48, v17, v34
	ds_bpermute_b32 v43, v16, v35
	ds_bpermute_b32 v49, v17, v35
	ds_bpermute_b32 v44, v16, v36
	ds_bpermute_b32 v50, v17, v36
	ds_bpermute_b32 v45, v16, v37
	ds_bpermute_b32 v51, v17, v37
	s_waitcnt lgkmcnt(0)
	v_add_f32_e32 v41, v40, v41
	v_sub_f32_e32 v12, v19, v42
	v_sub_f32_e32 v13, v18, v43
	v_rcp_f32_e32 v42, v40
	v_rcp_f32_e32 v43, v41
	s_nop 0
	v_fma_f32 v20, -v40, v42, 1.0
	v_fma_f32 v42, v20, v42, v42
	v_fma_f32 v20, -v41, v43, 1.0
	v_fma_f32 v43, v20, v43, v43
	v_mul_f32_e32 v8, 0xbf38aa3b, v42
	v_mul_f32_e32 v9, 0xbf38aa3b, v43
	v_mul_f32_e32 v44, v44, v42
	v_mul_f32_e32 v45, v45, v43
	v_mul_f32_e32 v10, 0x3e22f983, v44
	v_mul_f32_e32 v11, 0x3e22f983, v45
	v_add_f32_e32 v47, v46, v47
	v_sub_f32_e32 v2, v19, v48
	v_sub_f32_e32 v3, v18, v49
	v_rcp_f32_e32 v48, v46
	v_rcp_f32_e32 v49, v47
	s_nop 0
	v_fma_f32 v20, -v46, v48, 1.0
	v_fma_f32 v48, v20, v48, v48
	v_fma_f32 v20, -v47, v49, 1.0
	v_fma_f32 v49, v20, v49, v49
	v_mul_f32_e32 v28, 0xbf38aa3b, v48
	v_mul_f32_e32 v29, 0xbf38aa3b, v49
	v_mul_f32_e32 v50, v50, v48
	v_mul_f32_e32 v51, v51, v49
	v_mul_f32_e32 v30, 0x3e22f983, v50
	v_mul_f32_e32 v31, 0x3e22f983, v51
	s_getpc_b64 s[44:45]

.Lno_karg_touch:
	v_mul_f32_e32 v16, v12, v12
	v_add_f32_e32 v17, 0x3f800000, v12
	v_add_f32_e32 v18, 0x40000000, v12
	v_add_f32_e32 v19, 0x40400000, v12
	v_mul_f32_e32 v17, v17, v17
	v_mul_f32_e32 v18, v18, v18
	v_mul_f32_e32 v19, v19, v19
	v_mul_f32_e32 v20, v8, v16
	v_mul_f32_e32 v24, v9, v16
	v_mul_f32_e32 v21, v8, v17
	v_mul_f32_e32 v25, v9, v17
	v_mul_f32_e32 v22, v8, v18
	v_mul_f32_e32 v26, v9, v18
	v_mul_f32_e32 v23, v8, v19
	v_mul_f32_e32 v27, v9, v19
	v_exp_f32_e32 v20, v20
	v_exp_f32_e32 v21, v21
	v_exp_f32_e32 v22, v22
	v_exp_f32_e32 v23, v23
	v_exp_f32_e32 v24, v24
	v_exp_f32_e32 v25, v25
	v_exp_f32_e32 v26, v26
	v_exp_f32_e32 v27, v27
	v_cvt_pk_f16_f32 v32, v20, v21
	v_cvt_pk_f16_f32 v33, v22, v23
	v_cvt_pk_f16_f32 v64, v24, v25
	v_cvt_pk_f16_f32 v65, v26, v27
	v_add_f32_e32 v16, 0x40800000, v12
	v_add_f32_e32 v17, 0x40a00000, v12
	v_add_f32_e32 v18, 0x40c00000, v12
	v_add_f32_e32 v19, 0x40e00000, v12
	v_mul_f32_e32 v16, v16, v16
	v_mul_f32_e32 v17, v17, v17
	v_mul_f32_e32 v18, v18, v18
	v_mul_f32_e32 v19, v19, v19
	v_mul_f32_e32 v20, v8, v16
	v_mul_f32_e32 v24, v9, v16
	v_mul_f32_e32 v21, v8, v17
	v_mul_f32_e32 v25, v9, v17
	v_mul_f32_e32 v22, v8, v18
	v_mul_f32_e32 v26, v9, v18
	v_mul_f32_e32 v23, v8, v19
	v_mul_f32_e32 v27, v9, v19
	v_exp_f32_e32 v20, v20
	v_exp_f32_e32 v21, v21
	v_exp_f32_e32 v22, v22
	v_exp_f32_e32 v23, v23
	v_exp_f32_e32 v24, v24
	v_exp_f32_e32 v25, v25
	v_exp_f32_e32 v26, v26
	v_exp_f32_e32 v27, v27
	v_cvt_pk_f16_f32 v34, v20, v21
	v_cvt_pk_f16_f32 v35, v22, v23
	v_cvt_pk_f16_f32 v66, v24, v25
	v_cvt_pk_f16_f32 v67, v26, v27
	v_add_f32_e32 v16, 0x42000000, v12
	v_add_f32_e32 v17, 0x42040000, v12
	v_add_f32_e32 v18, 0x42080000, v12
	v_add_f32_e32 v19, 0x420c0000, v12
	v_mul_f32_e32 v16, v16, v16
	v_mul_f32_e32 v17, v17, v17
	v_mul_f32_e32 v18, v18, v18
	v_mul_f32_e32 v19, v19, v19
	v_mul_f32_e32 v20, v8, v16
	v_mul_f32_e32 v24, v9, v16
	v_mul_f32_e32 v21, v8, v17
	v_mul_f32_e32 v25, v9, v17
	v_mul_f32_e32 v22, v8, v18
	v_mul_f32_e32 v26, v9, v18
	v_mul_f32_e32 v23, v8, v19
	v_mul_f32_e32 v27, v9, v19
	v_exp_f32_e32 v20, v20
	v_exp_f32_e32 v21, v21
	v_exp_f32_e32 v22, v22
	v_exp_f32_e32 v23, v23
	v_exp_f32_e32 v24, v24
	v_exp_f32_e32 v25, v25
	v_exp_f32_e32 v26, v26
	v_exp_f32_e32 v27, v27
	v_cvt_pk_f16_f32 v36, v20, v21
	v_cvt_pk_f16_f32 v37, v22, v23
	v_cvt_pk_f16_f32 v68, v24, v25
	v_cvt_pk_f16_f32 v69, v26, v27
	v_add_f32_e32 v16, 0x42100000, v12
	v_add_f32_e32 v17, 0x42140000, v12
	v_add_f32_e32 v18, 0x42180000, v12
	v_add_f32_e32 v19, 0x421c0000, v12
	v_mul_f32_e32 v16, v16, v16
	v_mul_f32_e32 v17, v17, v17
	v_mul_f32_e32 v18, v18, v18
	v_mul_f32_e32 v19, v19, v19
	v_mul_f32_e32 v20, v8, v16
	v_mul_f32_e32 v24, v9, v16
	v_mul_f32_e32 v21, v8, v17
	v_mul_f32_e32 v25, v9, v17
	v_mul_f32_e32 v22, v8, v18
	v_mul_f32_e32 v26, v9, v18
	v_mul_f32_e32 v23, v8, v19
	v_mul_f32_e32 v27, v9, v19
	v_exp_f32_e32 v20, v20
	v_exp_f32_e32 v21, v21
	v_exp_f32_e32 v22, v22
	v_exp_f32_e32 v23, v23
	v_exp_f32_e32 v24, v24
	v_exp_f32_e32 v25, v25
	v_exp_f32_e32 v26, v26
	v_exp_f32_e32 v27, v27
	v_cvt_pk_f16_f32 v38, v20, v21
	v_cvt_pk_f16_f32 v39, v22, v23
	v_cvt_pk_f16_f32 v70, v24, v25
	v_cvt_pk_f16_f32 v71, v26, v27
	v_add_u32_e32 v6, 0x8000, v6
	global_load_dwordx4 v[176:179], v6, s[12:13] offset:0 nt
	global_load_dwordx4 v[180:183], v6, s[12:13] offset:1024 nt
	global_load_dwordx4 v[184:187], v6, s[12:13] offset:2048 nt
	global_load_dwordx4 v[188:191], v6, s[12:13] offset:3072 nt
	v_add_f32_e32 v16, 0x42800000, v12
	v_add_f32_e32 v17, 0x42820000, v12
	v_add_f32_e32 v18, 0x42840000, v12
	v_add_f32_e32 v19, 0x42860000, v12
	v_mul_f32_e32 v16, v16, v16
	v_mul_f32_e32 v17, v17, v17
	v_mul_f32_e32 v18, v18, v18
	v_mul_f32_e32 v19, v19, v19
	v_mul_f32_e32 v20, v8, v16
	v_mul_f32_e32 v24, v9, v16
	v_mul_f32_e32 v21, v8, v17
	v_mul_f32_e32 v25, v9, v17
	v_mul_f32_e32 v22, v8, v18
	v_mul_f32_e32 v26, v9, v18
	v_mul_f32_e32 v23, v8, v19
	v_mul_f32_e32 v27, v9, v19
	v_exp_f32_e32 v20, v20
	v_exp_f32_e32 v21, v21
	v_exp_f32_e32 v22, v22
	v_exp_f32_e32 v23, v23
	v_exp_f32_e32 v24, v24
	v_exp_f32_e32 v25, v25
	v_exp_f32_e32 v26, v26
	v_exp_f32_e32 v27, v27
	v_cvt_pk_f16_f32 v40, v20, v21
	v_cvt_pk_f16_f32 v41, v22, v23
	v_cvt_pk_f16_f32 v72, v24, v25
	v_cvt_pk_f16_f32 v73, v26, v27
	v_add_f32_e32 v16, 0x42880000, v12
	v_add_f32_e32 v17, 0x428a0000, v12
	v_add_f32_e32 v18, 0x428c0000, v12
	v_add_f32_e32 v19, 0x428e0000, v12
	v_mul_f32_e32 v16, v16, v16
	v_mul_f32_e32 v17, v17, v17
	v_mul_f32_e32 v18, v18, v18
	v_mul_f32_e32 v19, v19, v19
	v_mul_f32_e32 v20, v8, v16
	v_mul_f32_e32 v24, v9, v16
	v_mul_f32_e32 v21, v8, v17
	v_mul_f32_e32 v25, v9, v17
	v_mul_f32_e32 v22, v8, v18
	v_mul_f32_e32 v26, v9, v18
	v_mul_f32_e32 v23, v8, v19
	v_mul_f32_e32 v27, v9, v19
	v_exp_f32_e32 v20, v20
	v_exp_f32_e32 v21, v21
	v_exp_f32_e32 v22, v22
	v_exp_f32_e32 v23, v23
	v_exp_f32_e32 v24, v24
	v_exp_f32_e32 v25, v25
	v_exp_f32_e32 v26, v26
	v_exp_f32_e32 v27, v27
	v_cvt_pk_f16_f32 v42, v20, v21
	v_cvt_pk_f16_f32 v43, v22, v23
	v_cvt_pk_f16_f32 v74, v24, v25
	v_cvt_pk_f16_f32 v75, v26, v27
	v_add_f32_e32 v16, 0x42c00000, v12
	v_add_f32_e32 v17, 0x42c20000, v12
	v_add_f32_e32 v18, 0x42c40000, v12
	v_add_f32_e32 v19, 0x42c60000, v12
	v_mul_f32_e32 v16, v16, v16
	v_mul_f32_e32 v17, v17, v17
	v_mul_f32_e32 v18, v18, v18
	v_mul_f32_e32 v19, v19, v19
	v_mul_f32_e32 v20, v8, v16
	v_mul_f32_e32 v24, v9, v16
	v_mul_f32_e32 v21, v8, v17
	v_mul_f32_e32 v25, v9, v17
	v_mul_f32_e32 v22, v8, v18
	v_mul_f32_e32 v26, v9, v18
	v_mul_f32_e32 v23, v8, v19
	v_mul_f32_e32 v27, v9, v19
	v_exp_f32_e32 v20, v20
	v_exp_f32_e32 v21, v21
	v_exp_f32_e32 v22, v22
	v_exp_f32_e32 v23, v23
	v_exp_f32_e32 v24, v24
	v_exp_f32_e32 v25, v25
	v_exp_f32_e32 v26, v26
	v_exp_f32_e32 v27, v27
	v_cvt_pk_f16_f32 v44, v20, v21
	v_cvt_pk_f16_f32 v45, v22, v23
	v_cvt_pk_f16_f32 v76, v24, v25
	v_cvt_pk_f16_f32 v77, v26, v27
	v_add_f32_e32 v16, 0x42c80000, v12
	v_add_f32_e32 v17, 0x42ca0000, v12
	v_add_f32_e32 v18, 0x42cc0000, v12
	v_add_f32_e32 v19, 0x42ce0000, v12
	v_mul_f32_e32 v16, v16, v16
	v_mul_f32_e32 v17, v17, v17
	v_mul_f32_e32 v18, v18, v18
	v_mul_f32_e32 v19, v19, v19
	v_mul_f32_e32 v20, v8, v16
	v_mul_f32_e32 v24, v9, v16
	v_mul_f32_e32 v21, v8, v17
	v_mul_f32_e32 v25, v9, v17
	v_mul_f32_e32 v22, v8, v18
	v_mul_f32_e32 v26, v9, v18
	v_mul_f32_e32 v23, v8, v19
	v_mul_f32_e32 v27, v9, v19
	v_exp_f32_e32 v20, v20
	v_exp_f32_e32 v21, v21
	v_exp_f32_e32 v22, v22
	v_exp_f32_e32 v23, v23
	v_exp_f32_e32 v24, v24
	v_exp_f32_e32 v25, v25
	v_exp_f32_e32 v26, v26
	v_exp_f32_e32 v27, v27
	v_cvt_pk_f16_f32 v46, v20, v21
	v_cvt_pk_f16_f32 v47, v22, v23
	v_cvt_pk_f16_f32 v78, v24, v25
	v_cvt_pk_f16_f32 v79, v26, v27
	v_add_u32_e32 v6, 0x8000, v6
	global_load_dwordx4 v[192:195], v6, s[12:13] offset:0 nt
	global_load_dwordx4 v[196:199], v6, s[12:13] offset:1024 nt
	global_load_dwordx4 v[200:203], v6, s[12:13] offset:2048 nt
	global_load_dwordx4 v[204:207], v6, s[12:13] offset:3072 nt
	v_mul_f32_e32 v16, v2, v2
	v_add_f32_e32 v17, 0x3f800000, v2
	v_add_f32_e32 v18, 0x40000000, v2
	v_add_f32_e32 v19, 0x40400000, v2
	v_mul_f32_e32 v17, v17, v17
	v_mul_f32_e32 v18, v18, v18
	v_mul_f32_e32 v19, v19, v19
	v_mul_f32_e32 v20, v28, v16
	v_mul_f32_e32 v24, v29, v16
	v_mul_f32_e32 v21, v28, v17
	v_mul_f32_e32 v25, v29, v17
	v_mul_f32_e32 v22, v28, v18
	v_mul_f32_e32 v26, v29, v18
	v_mul_f32_e32 v23, v28, v19
	v_mul_f32_e32 v27, v29, v19
	v_exp_f32_e32 v20, v20
	v_exp_f32_e32 v21, v21
	v_exp_f32_e32 v22, v22
	v_exp_f32_e32 v23, v23
	v_exp_f32_e32 v24, v24
	v_exp_f32_e32 v25, v25
	v_exp_f32_e32 v26, v26
	v_exp_f32_e32 v27, v27
	v_cvt_pk_f16_f32 v48, v20, v21
	v_cvt_pk_f16_f32 v49, v22, v23
	v_cvt_pk_f16_f32 v80, v24, v25
	v_cvt_pk_f16_f32 v81, v26, v27
	v_add_f32_e32 v16, 0x40800000, v2
	v_add_f32_e32 v17, 0x40a00000, v2
	v_add_f32_e32 v18, 0x40c00000, v2
	v_add_f32_e32 v19, 0x40e00000, v2
	v_mul_f32_e32 v16, v16, v16
	v_mul_f32_e32 v17, v17, v17
	v_mul_f32_e32 v18, v18, v18
	v_mul_f32_e32 v19, v19, v19
	v_mul_f32_e32 v20, v28, v16
	v_mul_f32_e32 v24, v29, v16
	v_mul_f32_e32 v21, v28, v17
	v_mul_f32_e32 v25, v29, v17
	v_mul_f32_e32 v22, v28, v18
	v_mul_f32_e32 v26, v29, v18
	v_mul_f32_e32 v23, v28, v19
	v_mul_f32_e32 v27, v29, v19
	v_exp_f32_e32 v20, v20
	v_exp_f32_e32 v21, v21
	v_exp_f32_e32 v22, v22
	v_exp_f32_e32 v23, v23
	v_exp_f32_e32 v24, v24
	v_exp_f32_e32 v25, v25
	v_exp_f32_e32 v26, v26
	v_exp_f32_e32 v27, v27
	v_cvt_pk_f16_f32 v50, v20, v21
	v_cvt_pk_f16_f32 v51, v22, v23
	v_cvt_pk_f16_f32 v82, v24, v25
	v_cvt_pk_f16_f32 v83, v26, v27
	v_add_f32_e32 v16, 0x42000000, v2
	v_add_f32_e32 v17, 0x42040000, v2
	v_add_f32_e32 v18, 0x42080000, v2
	v_add_f32_e32 v19, 0x420c0000, v2
	v_mul_f32_e32 v16, v16, v16
	v_mul_f32_e32 v17, v17, v17
	v_mul_f32_e32 v18, v18, v18
	v_mul_f32_e32 v19, v19, v19
	v_mul_f32_e32 v20, v28, v16
	v_mul_f32_e32 v24, v29, v16
	v_mul_f32_e32 v21, v28, v17
	v_mul_f32_e32 v25, v29, v17
	v_mul_f32_e32 v22, v28, v18
	v_mul_f32_e32 v26, v29, v18
	v_mul_f32_e32 v23, v28, v19
	v_mul_f32_e32 v27, v29, v19
	v_exp_f32_e32 v20, v20
	v_exp_f32_e32 v21, v21
	v_exp_f32_e32 v22, v22
	v_exp_f32_e32 v23, v23
	v_exp_f32_e32 v24, v24
	v_exp_f32_e32 v25, v25
	v_exp_f32_e32 v26, v26
	v_exp_f32_e32 v27, v27
	v_cvt_pk_f16_f32 v52, v20, v21
	v_cvt_pk_f16_f32 v53, v22, v23
	v_cvt_pk_f16_f32 v84, v24, v25
	v_cvt_pk_f16_f32 v85, v26, v27
	v_add_f32_e32 v16, 0x42100000, v2
	v_add_f32_e32 v17, 0x42140000, v2
	v_add_f32_e32 v18, 0x42180000, v2
	v_add_f32_e32 v19, 0x421c0000, v2
	v_mul_f32_e32 v16, v16, v16
	v_mul_f32_e32 v17, v17, v17
	v_mul_f32_e32 v18, v18, v18
	v_mul_f32_e32 v19, v19, v19
	v_mul_f32_e32 v20, v28, v16
	v_mul_f32_e32 v24, v29, v16
	v_mul_f32_e32 v21, v28, v17
	v_mul_f32_e32 v25, v29, v17
	v_mul_f32_e32 v22, v28, v18
	v_mul_f32_e32 v26, v29, v18
	v_mul_f32_e32 v23, v28, v19
	v_mul_f32_e32 v27, v29, v19
	v_exp_f32_e32 v20, v20
	v_exp_f32_e32 v21, v21
	v_exp_f32_e32 v22, v22
	v_exp_f32_e32 v23, v23
	v_exp_f32_e32 v24, v24
	v_exp_f32_e32 v25, v25
	v_exp_f32_e32 v26, v26
	v_exp_f32_e32 v27, v27
	v_cvt_pk_f16_f32 v54, v20, v21
	v_cvt_pk_f16_f32 v55, v22, v23
	v_cvt_pk_f16_f32 v86, v24, v25
	v_cvt_pk_f16_f32 v87, v26, v27
	v_add_u32_e32 v6, 0x8000, v6
	global_load_dwordx4 v[208:211], v6, s[12:13] offset:0 nt
	global_load_dwordx4 v[212:215], v6, s[12:13] offset:1024 nt
	global_load_dwordx4 v[216:219], v6, s[12:13] offset:2048 nt
	global_load_dwordx4 v[220:223], v6, s[12:13] offset:3072 nt
	v_add_f32_e32 v16, 0x42800000, v2
	v_add_f32_e32 v17, 0x42820000, v2
	v_add_f32_e32 v18, 0x42840000, v2
	v_add_f32_e32 v19, 0x42860000, v2
	v_mul_f32_e32 v16, v16, v16
	v_mul_f32_e32 v17, v17, v17
	v_mul_f32_e32 v18, v18, v18
	v_mul_f32_e32 v19, v19, v19
	v_mul_f32_e32 v20, v28, v16
	v_mul_f32_e32 v24, v29, v16
	v_mul_f32_e32 v21, v28, v17
	v_mul_f32_e32 v25, v29, v17
	v_mul_f32_e32 v22, v28, v18
	v_mul_f32_e32 v26, v29, v18
	v_mul_f32_e32 v23, v28, v19
	v_mul_f32_e32 v27, v29, v19
	v_exp_f32_e32 v20, v20
	v_exp_f32_e32 v21, v21
	v_exp_f32_e32 v22, v22
	v_exp_f32_e32 v23, v23
	v_exp_f32_e32 v24, v24
	v_exp_f32_e32 v25, v25
	v_exp_f32_e32 v26, v26
	v_exp_f32_e32 v27, v27
	v_cvt_pk_f16_f32 v56, v20, v21
	v_cvt_pk_f16_f32 v57, v22, v23
	v_cvt_pk_f16_f32 v88, v24, v25
	v_cvt_pk_f16_f32 v89, v26, v27
	v_add_f32_e32 v16, 0x42880000, v2
	v_add_f32_e32 v17, 0x428a0000, v2
	v_add_f32_e32 v18, 0x428c0000, v2
	v_add_f32_e32 v19, 0x428e0000, v2
	v_mul_f32_e32 v16, v16, v16
	v_mul_f32_e32 v17, v17, v17
	v_mul_f32_e32 v18, v18, v18
	v_mul_f32_e32 v19, v19, v19
	v_mul_f32_e32 v20, v28, v16
	v_mul_f32_e32 v24, v29, v16
	v_mul_f32_e32 v21, v28, v17
	v_mul_f32_e32 v25, v29, v17
	v_mul_f32_e32 v22, v28, v18
	v_mul_f32_e32 v26, v29, v18
	v_mul_f32_e32 v23, v28, v19
	v_mul_f32_e32 v27, v29, v19
	v_exp_f32_e32 v20, v20
	v_exp_f32_e32 v21, v21
	v_exp_f32_e32 v22, v22
	v_exp_f32_e32 v23, v23
	v_exp_f32_e32 v24, v24
	v_exp_f32_e32 v25, v25
	v_exp_f32_e32 v26, v26
	v_exp_f32_e32 v27, v27
	v_cvt_pk_f16_f32 v58, v20, v21
	v_cvt_pk_f16_f32 v59, v22, v23
	v_cvt_pk_f16_f32 v90, v24, v25
	v_cvt_pk_f16_f32 v91, v26, v27
	v_add_f32_e32 v16, 0x42c00000, v2
	v_add_f32_e32 v17, 0x42c20000, v2
	v_add_f32_e32 v18, 0x42c40000, v2
	v_add_f32_e32 v19, 0x42c60000, v2
	v_mul_f32_e32 v16, v16, v16
	v_mul_f32_e32 v17, v17, v17
	v_mul_f32_e32 v18, v18, v18
	v_mul_f32_e32 v19, v19, v19
	v_mul_f32_e32 v20, v28, v16
	v_mul_f32_e32 v24, v29, v16
	v_mul_f32_e32 v21, v28, v17
	v_mul_f32_e32 v25, v29, v17
	v_mul_f32_e32 v22, v28, v18
	v_mul_f32_e32 v26, v29, v18
	v_mul_f32_e32 v23, v28, v19
	v_mul_f32_e32 v27, v29, v19
	v_exp_f32_e32 v20, v20
	v_exp_f32_e32 v21, v21
	v_exp_f32_e32 v22, v22
	v_exp_f32_e32 v23, v23
	v_exp_f32_e32 v24, v24
	v_exp_f32_e32 v25, v25
	v_exp_f32_e32 v26, v26
	v_exp_f32_e32 v27, v27
	v_cvt_pk_f16_f32 v60, v20, v21
	v_cvt_pk_f16_f32 v61, v22, v23
	v_cvt_pk_f16_f32 v92, v24, v25
	v_cvt_pk_f16_f32 v93, v26, v27
	v_add_f32_e32 v16, 0x42c80000, v2
	v_add_f32_e32 v17, 0x42ca0000, v2
	v_add_f32_e32 v18, 0x42cc0000, v2
	v_add_f32_e32 v19, 0x42ce0000, v2
	v_mul_f32_e32 v16, v16, v16
	v_mul_f32_e32 v17, v17, v17
	v_mul_f32_e32 v18, v18, v18
	v_mul_f32_e32 v19, v19, v19
	v_mul_f32_e32 v20, v28, v16
	v_mul_f32_e32 v24, v29, v16
	v_mul_f32_e32 v21, v28, v17
	v_mul_f32_e32 v25, v29, v17
	v_mul_f32_e32 v22, v28, v18
	v_mul_f32_e32 v26, v29, v18
	v_mul_f32_e32 v23, v28, v19
	v_mul_f32_e32 v27, v29, v19
	v_exp_f32_e32 v20, v20
	v_exp_f32_e32 v21, v21
	v_exp_f32_e32 v22, v22
	v_exp_f32_e32 v23, v23
	v_exp_f32_e32 v24, v24
	v_exp_f32_e32 v25, v25
	v_exp_f32_e32 v26, v26
	v_exp_f32_e32 v27, v27
	v_cvt_pk_f16_f32 v62, v20, v21
	v_cvt_pk_f16_f32 v63, v22, v23
	v_cvt_pk_f16_f32 v94, v24, v25
	v_cvt_pk_f16_f32 v95, v26, v27
	v_add_u32_e32 v6, 0x8000, v6
	global_load_dwordx4 v[224:227], v6, s[12:13] offset:0 nt
	global_load_dwordx4 v[228:231], v6, s[12:13] offset:1024 nt
	global_load_dwordx4 v[232:235], v6, s[12:13] offset:2048 nt
	global_load_dwordx4 v[236:239], v6, s[12:13] offset:3072 nt
	v_mul_f32_e32 v16, v13, v13
	v_add_f32_e32 v17, 0x3f800000, v13
	v_add_f32_e32 v18, 0x40000000, v13
	v_add_f32_e32 v19, 0x40400000, v13
	v_mul_f32_e32 v17, v17, v17
	v_mul_f32_e32 v18, v18, v18
	v_mul_f32_e32 v19, v19, v19
	v_mul_f32_e32 v20, v8, v16
	v_mul_f32_e32 v24, v9, v16
	v_mul_f32_e32 v21, v8, v17
	v_mul_f32_e32 v25, v9, v17
	v_mul_f32_e32 v22, v8, v18
	v_mul_f32_e32 v26, v9, v18
	v_mul_f32_e32 v23, v8, v19
	v_mul_f32_e32 v27, v9, v19
	v_exp_f32_e32 v20, v20
	v_exp_f32_e32 v21, v21
	v_exp_f32_e32 v22, v22
	v_exp_f32_e32 v23, v23
	v_exp_f32_e32 v24, v24
	v_exp_f32_e32 v25, v25
	v_exp_f32_e32 v26, v26
	v_exp_f32_e32 v27, v27
	v_mul_f32_e32 v96, v10, v20
	v_mul_f32_e32 v97, v10, v21
	v_mul_f32_e32 v98, v10, v22
	v_mul_f32_e32 v99, v10, v23
	v_mul_f32_e32 v112, v11, v24
	v_mul_f32_e32 v113, v11, v25
	v_mul_f32_e32 v114, v11, v26
	v_mul_f32_e32 v115, v11, v27
	v_add_f32_e32 v16, 0x41800000, v13
	v_add_f32_e32 v17, 0x41880000, v13
	v_add_f32_e32 v18, 0x41900000, v13
	v_add_f32_e32 v19, 0x41980000, v13
	v_mul_f32_e32 v16, v16, v16
	v_mul_f32_e32 v17, v17, v17
	v_mul_f32_e32 v18, v18, v18
	v_mul_f32_e32 v19, v19, v19
	v_mul_f32_e32 v20, v8, v16
	v_mul_f32_e32 v24, v9, v16
	v_mul_f32_e32 v21, v8, v17
	v_mul_f32_e32 v25, v9, v17
	v_mul_f32_e32 v22, v8, v18
	v_mul_f32_e32 v26, v9, v18
	v_mul_f32_e32 v23, v8, v19
	v_mul_f32_e32 v27, v9, v19
	v_exp_f32_e32 v20, v20
	v_exp_f32_e32 v21, v21
	v_exp_f32_e32 v22, v22
	v_exp_f32_e32 v23, v23
	v_exp_f32_e32 v24, v24
	v_exp_f32_e32 v25, v25
	v_exp_f32_e32 v26, v26
	v_exp_f32_e32 v27, v27
	v_mul_f32_e32 v100, v10, v20
	v_mul_f32_e32 v101, v10, v21
	v_mul_f32_e32 v102, v10, v22
	v_mul_f32_e32 v103, v10, v23
	v_mul_f32_e32 v116, v11, v24
	v_mul_f32_e32 v117, v11, v25
	v_mul_f32_e32 v118, v11, v26
	v_mul_f32_e32 v119, v11, v27
	v_add_u32_e32 v6, 0x8000, v6
	global_load_dwordx4 v[240:243], v6, s[12:13] offset:0 nt
	global_load_dwordx4 v[244:247], v6, s[12:13] offset:1024 nt
	global_load_dwordx4 v[248:251], v6, s[12:13] offset:2048 nt
	global_load_dwordx4 v[252:255], v6, s[12:13] offset:3072 nt
	v_mul_f32_e32 v16, v3, v3
	v_add_f32_e32 v17, 0x3f800000, v3
	v_add_f32_e32 v18, 0x40000000, v3
	v_add_f32_e32 v19, 0x40400000, v3
	v_mul_f32_e32 v17, v17, v17
	v_mul_f32_e32 v18, v18, v18
	v_mul_f32_e32 v19, v19, v19
	v_mul_f32_e32 v20, v28, v16
	v_mul_f32_e32 v24, v29, v16
	v_mul_f32_e32 v21, v28, v17
	v_mul_f32_e32 v25, v29, v17
	v_mul_f32_e32 v22, v28, v18
	v_mul_f32_e32 v26, v29, v18
	v_mul_f32_e32 v23, v28, v19
	v_mul_f32_e32 v27, v29, v19
	v_exp_f32_e32 v20, v20
	v_exp_f32_e32 v21, v21
	v_exp_f32_e32 v22, v22
	v_exp_f32_e32 v23, v23
	v_exp_f32_e32 v24, v24
	v_exp_f32_e32 v25, v25
	v_exp_f32_e32 v26, v26
	v_exp_f32_e32 v27, v27
	v_mul_f32_e32 v104, v30, v20
	v_mul_f32_e32 v105, v30, v21
	v_mul_f32_e32 v106, v30, v22
	v_mul_f32_e32 v107, v30, v23
	v_mul_f32_e32 v120, v31, v24
	v_mul_f32_e32 v121, v31, v25
	v_mul_f32_e32 v122, v31, v26
	v_mul_f32_e32 v123, v31, v27
	v_add_f32_e32 v16, 0x41800000, v3
	v_add_f32_e32 v17, 0x41880000, v3
	v_add_f32_e32 v18, 0x41900000, v3
	v_add_f32_e32 v19, 0x41980000, v3
	v_mul_f32_e32 v16, v16, v16
	v_mul_f32_e32 v17, v17, v17
	v_mul_f32_e32 v18, v18, v18
	v_mul_f32_e32 v19, v19, v19
	v_mul_f32_e32 v20, v28, v16
	v_mul_f32_e32 v24, v29, v16
	v_mul_f32_e32 v21, v28, v17
	v_mul_f32_e32 v25, v29, v17
	v_mul_f32_e32 v22, v28, v18
	v_mul_f32_e32 v26, v29, v18
	v_mul_f32_e32 v23, v28, v19
	v_mul_f32_e32 v27, v29, v19
	v_exp_f32_e32 v20, v20
	v_exp_f32_e32 v21, v21
	v_exp_f32_e32 v22, v22
	v_exp_f32_e32 v23, v23
	v_exp_f32_e32 v24, v24
	v_exp_f32_e32 v25, v25
	v_exp_f32_e32 v26, v26
	v_exp_f32_e32 v27, v27
	v_mul_f32_e32 v108, v30, v20
	v_mul_f32_e32 v109, v30, v21
	v_mul_f32_e32 v110, v30, v22
	v_mul_f32_e32 v111, v30, v23
	v_mul_f32_e32 v124, v31, v24
	v_mul_f32_e32 v125, v31, v25
	v_mul_f32_e32 v126, v31, v26
	v_mul_f32_e32 v127, v31, v27
	s_waitcnt vmcnt(28)
	v_add_f32_e32 v128, v128, v129
	v_add_f32_e32 v130, v130, v131
	v_add_f32_e32 v132, v132, v133
	v_add_f32_e32 v134, v134, v135
	v_add_f32_e32 v136, v136, v137
	v_add_f32_e32 v138, v138, v139
	v_add_f32_e32 v140, v140, v141
	v_add_f32_e32 v142, v142, v143
	v_add_f32_e32 v128, v128, v130
	v_add_f32_e32 v132, v132, v134
	v_add_f32_e32 v136, v136, v138
	v_add_f32_e32 v140, v140, v142
	v_cndmask_b32_e64 v130, v128, v132, s[30:31]
	v_cndmask_b32_e64 v134, v136, v140, s[30:31]
	v_cndmask_b32_e64 v129, v132, v128, s[30:31]
	v_cndmask_b32_e64 v133, v140, v136, s[30:31]
	v_add_f32_dpp v129, v130, v129 quad_perm:[1,0,3,2] row_mask:0xf bank_mask:0xf bound_ctrl:1
	v_add_f32_dpp v133, v134, v133 quad_perm:[1,0,3,2] row_mask:0xf bank_mask:0xf bound_ctrl:1
	v_cndmask_b32_e64 v135, v129, v133, s[32:33]
	v_cndmask_b32_e64 v131, v133, v129, s[32:33]
	s_nop 1
	v_add_f32_dpp v131, v135, v131 quad_perm:[2,3,0,1] row_mask:0xf bank_mask:0xf bound_ctrl:1
	v_cvt_f16_f32_e32 v131, v131
	ds_write_b16 v14, v131 offset:0
	s_waitcnt vmcnt(24)
	v_add_f32_e32 v144, v144, v145
	v_add_f32_e32 v146, v146, v147
	v_add_f32_e32 v148, v148, v149
	v_add_f32_e32 v150, v150, v151
	v_add_f32_e32 v152, v152, v153
	v_add_f32_e32 v154, v154, v155
	v_add_f32_e32 v156, v156, v157
	v_add_f32_e32 v158, v158, v159
	v_add_f32_e32 v144, v144, v146
	v_add_f32_e32 v148, v148, v150
	v_add_f32_e32 v152, v152, v154
	v_add_f32_e32 v156, v156, v158
	v_cndmask_b32_e64 v146, v144, v148, s[30:31]
	v_cndmask_b32_e64 v150, v152, v156, s[30:31]
	v_cndmask_b32_e64 v145, v148, v144, s[30:31]
	v_cndmask_b32_e64 v149, v156, v152, s[30:31]
	v_add_f32_dpp v145, v146, v145 quad_perm:[1,0,3,2] row_mask:0xf bank_mask:0xf bound_ctrl:1
	v_add_f32_dpp v149, v150, v149 quad_perm:[1,0,3,2] row_mask:0xf bank_mask:0xf bound_ctrl:1
	v_cndmask_b32_e64 v151, v145, v149, s[32:33]
	v_cndmask_b32_e64 v147, v149, v145, s[32:33]
	s_nop 1
	v_add_f32_dpp v147, v151, v147 quad_perm:[2,3,0,1] row_mask:0xf bank_mask:0xf bound_ctrl:1
	v_cvt_f16_f32_e32 v147, v147
	ds_write_b16 v14, v147 offset:1088
	s_waitcnt vmcnt(20)
	v_add_f32_e32 v160, v160, v161
	v_add_f32_e32 v162, v162, v163
	v_add_f32_e32 v164, v164, v165
	v_add_f32_e32 v166, v166, v167
	v_add_f32_e32 v168, v168, v169
	v_add_f32_e32 v170, v170, v171
	v_add_f32_e32 v172, v172, v173
	v_add_f32_e32 v174, v174, v175
	v_add_f32_e32 v160, v160, v162
	v_add_f32_e32 v164, v164, v166
	v_add_f32_e32 v168, v168, v170
	v_add_f32_e32 v172, v172, v174
	v_cndmask_b32_e64 v162, v160, v164, s[30:31]
	v_cndmask_b32_e64 v166, v168, v172, s[30:31]
	v_cndmask_b32_e64 v161, v164, v160, s[30:31]
	v_cndmask_b32_e64 v165, v172, v168, s[30:31]
	v_add_f32_dpp v161, v162, v161 quad_perm:[1,0,3,2] row_mask:0xf bank_mask:0xf bound_ctrl:1
	v_add_f32_dpp v165, v166, v165 quad_perm:[1,0,3,2] row_mask:0xf bank_mask:0xf bound_ctrl:1
	v_cndmask_b32_e64 v167, v161, v165, s[32:33]
	v_cndmask_b32_e64 v163, v165, v161, s[32:33]
	s_nop 1
	v_add_f32_dpp v163, v167, v163 quad_perm:[2,3,0,1] row_mask:0xf bank_mask:0xf bound_ctrl:1
	v_cvt_f16_f32_e32 v163, v163
	ds_write_b16 v14, v163 offset:2176
	s_waitcnt vmcnt(16)
	v_add_f32_e32 v176, v176, v177
	v_add_f32_e32 v178, v178, v179
	v_add_f32_e32 v180, v180, v181
	v_add_f32_e32 v182, v182, v183
	v_add_f32_e32 v184, v184, v185
	v_add_f32_e32 v186, v186, v187
	v_add_f32_e32 v188, v188, v189
	v_add_f32_e32 v190, v190, v191
	v_add_f32_e32 v176, v176, v178
	v_add_f32_e32 v180, v180, v182
	v_add_f32_e32 v184, v184, v186
	v_add_f32_e32 v188, v188, v190
	v_cndmask_b32_e64 v178, v176, v180, s[30:31]
	v_cndmask_b32_e64 v182, v184, v188, s[30:31]
	v_cndmask_b32_e64 v177, v180, v176, s[30:31]
	v_cndmask_b32_e64 v181, v188, v184, s[30:31]
	v_add_f32_dpp v177, v178, v177 quad_perm:[1,0,3,2] row_mask:0xf bank_mask:0xf bound_ctrl:1
	v_add_f32_dpp v181, v182, v181 quad_perm:[1,0,3,2] row_mask:0xf bank_mask:0xf bound_ctrl:1
	v_cndmask_b32_e64 v183, v177, v181, s[32:33]
	v_cndmask_b32_e64 v179, v181, v177, s[32:33]
	s_nop 1
	v_add_f32_dpp v179, v183, v179 quad_perm:[2,3,0,1] row_mask:0xf bank_mask:0xf bound_ctrl:1
	v_cvt_f16_f32_e32 v179, v179
	ds_write_b16 v14, v179 offset:3264
	s_mov_b32 s29, 0
	v_mov_b32_e32 v160, 0
	v_mov_b32_e32 v161, 0
	v_mov_b32_e32 v162, 0
	v_mov_b32_e32 v163, 0
	s_lshl_b32 s6, s6, 6
	s_add_i32 s6, s6, s7
	s_lshl_b32 s6, s6, 10
	v_add_u32_e32 v5, s6, v5
	s_branch .Lpass
